# v43 + trimmed scan: per-segment counters in X row padding (no address VALU), compact pass 2, multiply-free flush
# speedup vs baseline: 1.0391x; 1.0134x over previous
_Z7vq_mainPKfPKiS0_PfPhPdPi:
	s_load_dwordx4 s[4:7], s[0:1], 0x0
	s_load_dwordx2 s[22:23], s[0:1], 0x10
	s_load_dwordx2 s[20:21], s[0:1], 0x18
	s_load_dwordx4 s[12:15], s[0:1], 0x20
	s_load_dwordx2 s[10:11], s[0:1], 0x30
	s_and_b32 s3, s2, 7
	s_lshl_b32 s3, s3, 6
	s_lshr_b32 s16, s2, 3
	s_add_i32 s16, s16, s3
	s_lshr_b32 s18, s16, 5
	s_mov_b32 s19, 0
	s_and_b32 s28, s16, 31
	s_lshl_b32 s28, s28, 4
	s_add_i32 s29, s28, 1
	v_readfirstlane_b32 s17, v0
	v_and_b32_e32 v1, 63, v0
	v_lshlrev_b32_e32 v66, 4, v0
	s_lshr_b32 s17, s17, 6
	s_lshl_b32 s24, s17, 4
	s_lshl_b32 s30, s18, 15
	s_lshl_b32 s31, s18, 23
	v_add_u32_e32 v67, 0x1000, v66
	v_add_u32_e32 v68, 0x2000, v66
	v_add_u32_e32 v69, 0x3000, v66
	v_add_u32_e32 v70, 0x4000, v66
	v_add_u32_e32 v71, 0x5000, v66
	v_add_u32_e32 v72, 0x6000, v66
	v_add_u32_e32 v73, 0x7000, v66
	s_movk_i32 s100, 0x810
	s_mov_b32 s101, 0x8100
	s_mul_i32 s36, s29, 0x810
	v_mov_b32_e32 v141, s36
	v_sub_u32_e32 v141, 0, v141
	s_waitcnt lgkmcnt(0)
	s_add_u32 s34, s6, s30
	s_addc_u32 s35, s7, 0
	s_add_u32 s32, s4, s31
	s_addc_u32 s33, s5, 0
	global_load_dwordx4 v[74:77], v66, s[34:35]
	global_load_dwordx4 v[78:81], v67, s[34:35]
	global_load_dwordx4 v[82:85], v68, s[34:35]
	global_load_dwordx4 v[86:89], v69, s[34:35]
	global_load_dwordx4 v[90:93], v70, s[34:35]
	global_load_dwordx4 v[94:97], v71, s[34:35]
	global_load_dwordx4 v[98:101], v72, s[34:35]
	global_load_dwordx4 v[102:105], v73, s[34:35]
	v_and_b32_e32 v150, 15, v0
	v_or_b32_e32 v150, s24, v150
	v_and_b32_e32 v151, 48, v0
	v_lshl_or_b32 v150, v150, 10, v151
	global_load_dwordx4 v[62:65], v150, s[22:23] offset:0
	global_load_dwordx4 v[58:61], v150, s[22:23] offset:64
	global_load_dwordx4 v[54:57], v150, s[22:23] offset:128
	global_load_dwordx4 v[50:53], v150, s[22:23] offset:192
	global_load_dwordx4 v[46:49], v150, s[22:23] offset:256
	global_load_dwordx4 v[42:45], v150, s[22:23] offset:320
	global_load_dwordx4 v[38:41], v150, s[22:23] offset:384
	global_load_dwordx4 v[34:37], v150, s[22:23] offset:448
	global_load_dwordx4 v[30:33], v150, s[22:23] offset:512
	global_load_dwordx4 v[26:29], v150, s[22:23] offset:576
	global_load_dwordx4 v[22:25], v150, s[22:23] offset:640
	global_load_dwordx4 v[18:21], v150, s[22:23] offset:704
	global_load_dwordx4 v[14:17], v150, s[22:23] offset:768
	global_load_dwordx4 v[10:13], v150, s[22:23] offset:832
	global_load_dwordx4 v[6:9], v150, s[22:23] offset:896
	global_load_dwordx4 v[2:5], v150, s[22:23] offset:960
	v_mov_b32_e32 v142, 1
	v_mov_b32_e32 v143, 4
	v_mov_b32_e32 v144, 0x11100
	v_lshlrev_b32_e32 v145, 8, v0
	v_lshlrev_b32_e32 v148, 3, v0
	v_mov_b32_e32 v152, 0
	v_mov_b32_e32 v153, 0
	ds_write_b64 v148, v[152:153] offset:32768
	ds_write_b64 v148, v[152:153] offset:34832
	ds_write_b64 v148, v[152:153] offset:36896
	ds_write_b64 v148, v[152:153] offset:38960
	ds_write_b64 v148, v[152:153] offset:41024
	ds_write_b64 v148, v[152:153] offset:43088
	ds_write_b64 v148, v[152:153] offset:45152
	ds_write_b64 v148, v[152:153] offset:47216
	ds_write_b64 v148, v[152:153] offset:49280
	ds_write_b64 v148, v[152:153] offset:51344
	ds_write_b64 v148, v[152:153] offset:53408
	ds_write_b64 v148, v[152:153] offset:55472
	ds_write_b64 v148, v[152:153] offset:57536
	ds_write_b64 v148, v[152:153] offset:59600
	ds_write_b64 v148, v[152:153] offset:61664
	ds_write_b64 v148, v[152:153] offset:63728
	v_cmp_gt_u32_e32 vcc, 16, v0
	s_and_saveexec_b64 s[30:31], vcc
	v_mul_u32_u24_e32 v151, 0x810, v0
	ds_write_b64 v151, v[152:153] offset:34816
	v_mov_b32_e32 v150, 0x11540
	v_mov_b32_e32 v149, 8
	ds_write_b32 v150, v149
	s_mov_b64 exec, s[30:31]
	s_waitcnt lgkmcnt(0)
	s_barrier
	s_waitcnt vmcnt(16)
	v_mad_u32_u24 v74, v74, s100, v141
	v_mad_u32_u24 v75, v75, s100, v141
	v_mad_u32_u24 v76, v76, s100, v141
	v_mad_u32_u24 v77, v77, s100, v141
	v_mad_u32_u24 v78, v78, s100, v141
	v_mad_u32_u24 v79, v79, s100, v141
	v_mad_u32_u24 v80, v80, s100, v141
	v_mad_u32_u24 v81, v81, s100, v141
	v_mad_u32_u24 v82, v82, s100, v141
	v_mad_u32_u24 v83, v83, s100, v141
	v_mad_u32_u24 v84, v84, s100, v141
	v_mad_u32_u24 v85, v85, s100, v141
	v_mad_u32_u24 v86, v86, s100, v141
	v_mad_u32_u24 v87, v87, s100, v141
	v_mad_u32_u24 v88, v88, s100, v141
	v_mad_u32_u24 v89, v89, s100, v141
	v_mad_u32_u24 v90, v90, s100, v141
	v_mad_u32_u24 v91, v91, s100, v141
	v_mad_u32_u24 v92, v92, s100, v141
	v_mad_u32_u24 v93, v93, s100, v141
	v_mad_u32_u24 v94, v94, s100, v141
	v_mad_u32_u24 v95, v95, s100, v141
	v_mad_u32_u24 v96, v96, s100, v141
	v_mad_u32_u24 v97, v97, s100, v141
	v_mad_u32_u24 v98, v98, s100, v141
	v_mad_u32_u24 v99, v99, s100, v141
	v_mad_u32_u24 v100, v100, s100, v141
	v_mad_u32_u24 v101, v101, s100, v141
	v_mad_u32_u24 v102, v102, s100, v141
	v_mad_u32_u24 v103, v103, s100, v141
	v_mad_u32_u24 v104, v104, s100, v141
	v_mad_u32_u24 v105, v105, s100, v141
	v_cmp_gt_u32_e64 s[36:37], s101, v74
	v_cmp_gt_u32_e64 s[38:39], s101, v75
	v_cmp_gt_u32_e64 s[40:41], s101, v76
	v_cmp_gt_u32_e64 s[42:43], s101, v77
	v_cmp_gt_u32_e64 s[44:45], s101, v78
	v_cmp_gt_u32_e64 s[46:47], s101, v79
	v_cmp_gt_u32_e64 s[48:49], s101, v80
	v_cmp_gt_u32_e64 s[50:51], s101, v81
	v_cmp_gt_u32_e64 s[52:53], s101, v82
	v_cmp_gt_u32_e64 s[54:55], s101, v83
	v_cmp_gt_u32_e64 s[56:57], s101, v84
	v_cmp_gt_u32_e64 s[58:59], s101, v85
	v_cmp_gt_u32_e64 s[60:61], s101, v86
	v_cmp_gt_u32_e64 s[62:63], s101, v87
	v_cmp_gt_u32_e64 s[64:65], s101, v88
	v_cmp_gt_u32_e64 s[66:67], s101, v89
	v_cmp_gt_u32_e64 s[68:69], s101, v90
	v_cmp_gt_u32_e64 s[70:71], s101, v91
	v_cmp_gt_u32_e64 s[72:73], s101, v92
	v_cmp_gt_u32_e64 s[74:75], s101, v93
	v_cmp_gt_u32_e64 s[76:77], s101, v94
	v_cmp_gt_u32_e64 s[78:79], s101, v95
	v_cmp_gt_u32_e64 s[80:81], s101, v96
	v_cmp_gt_u32_e64 s[82:83], s101, v97
	v_cmp_gt_u32_e64 s[84:85], s101, v98
	v_cmp_gt_u32_e64 s[86:87], s101, v99
	v_cmp_gt_u32_e64 s[88:89], s101, v100
	v_cmp_gt_u32_e64 s[90:91], s101, v101
	v_cmp_gt_u32_e64 s[92:93], s101, v102
	v_cmp_gt_u32_e64 s[94:95], s101, v103
	v_cmp_gt_u32_e64 s[96:97], s101, v104
	v_cmp_gt_u32_e64 s[98:99], s101, v105
	s_mov_b64 exec, s[36:37]
	ds_add_u32 v74, v142 offset:34816
	s_mov_b64 exec, s[38:39]
	ds_add_u32 v75, v142 offset:34816
	s_mov_b64 exec, s[40:41]
	ds_add_u32 v76, v142 offset:34816
	s_mov_b64 exec, s[42:43]
	ds_add_u32 v77, v142 offset:34816
	s_mov_b64 exec, s[44:45]
	ds_add_u32 v78, v142 offset:34816
	s_mov_b64 exec, s[46:47]
	ds_add_u32 v79, v142 offset:34816
	s_mov_b64 exec, s[48:49]
	ds_add_u32 v80, v142 offset:34816
	s_mov_b64 exec, s[50:51]
	ds_add_u32 v81, v142 offset:34816
	s_mov_b64 exec, s[52:53]
	ds_add_u32 v82, v142 offset:34816
	s_mov_b64 exec, s[54:55]
	ds_add_u32 v83, v142 offset:34816
	s_mov_b64 exec, s[56:57]
	ds_add_u32 v84, v142 offset:34816
	s_mov_b64 exec, s[58:59]
	ds_add_u32 v85, v142 offset:34816
	s_mov_b64 exec, s[60:61]
	ds_add_u32 v86, v142 offset:34816
	s_mov_b64 exec, s[62:63]
	ds_add_u32 v87, v142 offset:34816
	s_mov_b64 exec, s[64:65]
	ds_add_u32 v88, v142 offset:34816
	s_mov_b64 exec, s[66:67]
	ds_add_u32 v89, v142 offset:34816
	s_mov_b64 exec, s[68:69]
	ds_add_u32 v90, v142 offset:34816
	s_mov_b64 exec, s[70:71]
	ds_add_u32 v91, v142 offset:34816
	s_mov_b64 exec, s[72:73]
	ds_add_u32 v92, v142 offset:34816
	s_mov_b64 exec, s[74:75]
	ds_add_u32 v93, v142 offset:34816
	s_mov_b64 exec, s[76:77]
	ds_add_u32 v94, v142 offset:34816
	s_mov_b64 exec, s[78:79]
	ds_add_u32 v95, v142 offset:34816
	s_mov_b64 exec, s[80:81]
	ds_add_u32 v96, v142 offset:34816
	s_mov_b64 exec, s[82:83]
	ds_add_u32 v97, v142 offset:34816
	s_mov_b64 exec, s[84:85]
	ds_add_u32 v98, v142 offset:34816
	s_mov_b64 exec, s[86:87]
	ds_add_u32 v99, v142 offset:34816
	s_mov_b64 exec, s[88:89]
	ds_add_u32 v100, v142 offset:34816
	s_mov_b64 exec, s[90:91]
	ds_add_u32 v101, v142 offset:34816
	s_mov_b64 exec, s[92:93]
	ds_add_u32 v102, v142 offset:34816
	s_mov_b64 exec, s[94:95]
	ds_add_u32 v103, v142 offset:34816
	s_mov_b64 exec, s[96:97]
	ds_add_u32 v104, v142 offset:34816
	s_mov_b64 exec, s[98:99]
	ds_add_u32 v105, v142 offset:34816
	s_mov_b64 exec, -1
	s_waitcnt lgkmcnt(0)
	s_barrier
	v_and_b32_e32 v67, 15, v0
	v_mul_u32_u24_e32 v67, 0x810, v67
	ds_read_b32 v68, v67 offset:34816
	s_waitcnt lgkmcnt(0)
	v_mov_b32_e32 v69, v68
	s_nop 1
	v_add_u32_dpp v69, v69, v69 row_shr:1 row_mask:0xf bank_mask:0xf bound_ctrl:1
	s_nop 1
	v_add_u32_dpp v69, v69, v69 row_shr:2 row_mask:0xf bank_mask:0xf bound_ctrl:1
	s_nop 1
	v_add_u32_dpp v69, v69, v69 row_shr:4 row_mask:0xf bank_mask:0xf bound_ctrl:1
	s_nop 1
	v_add_u32_dpp v69, v69, v69 row_shr:8 row_mask:0xf bank_mask:0xf bound_ctrl:1
	s_nop 1
	v_sub_u32_e32 v70, v69, v68
	v_lshlrev_b32_e32 v70, 2, v70
	v_readlane_b32 s8, v69, 15
	s_cmp_lg_u32 s17, 0
	s_cbranch_scc1 .Lfront_nocursor
	v_cmp_gt_u32_e32 vcc, 16, v1
	s_and_saveexec_b64 s[30:31], vcc
	ds_write_b32 v67, v70 offset:34820
	s_mov_b64 exec, s[30:31]
.Lfront_nocursor:
	s_waitcnt lgkmcnt(0)
	s_barrier
	s_mov_b64 exec, s[36:37]
	ds_add_rtn_u32 v106, v74, v143 offset:34820
	s_mov_b64 exec, s[38:39]
	ds_add_rtn_u32 v107, v75, v143 offset:34820
	s_mov_b64 exec, s[40:41]
	ds_add_rtn_u32 v108, v76, v143 offset:34820
	s_mov_b64 exec, s[42:43]
	ds_add_rtn_u32 v109, v77, v143 offset:34820
	s_mov_b64 exec, s[44:45]
	ds_add_rtn_u32 v110, v78, v143 offset:34820
	s_mov_b64 exec, s[46:47]
	ds_add_rtn_u32 v111, v79, v143 offset:34820
	s_mov_b64 exec, s[48:49]
	ds_add_rtn_u32 v112, v80, v143 offset:34820
	s_mov_b64 exec, s[50:51]
	ds_add_rtn_u32 v113, v81, v143 offset:34820
	s_mov_b64 exec, s[52:53]
	ds_add_rtn_u32 v114, v82, v143 offset:34820
	s_mov_b64 exec, s[54:55]
	ds_add_rtn_u32 v115, v83, v143 offset:34820
	s_mov_b64 exec, s[56:57]
	ds_add_rtn_u32 v116, v84, v143 offset:34820
	s_mov_b64 exec, s[58:59]
	ds_add_rtn_u32 v117, v85, v143 offset:34820
	s_mov_b64 exec, s[60:61]
	ds_add_rtn_u32 v118, v86, v143 offset:34820
	s_mov_b64 exec, s[62:63]
	ds_add_rtn_u32 v119, v87, v143 offset:34820
	s_mov_b64 exec, s[64:65]
	ds_add_rtn_u32 v120, v88, v143 offset:34820
	s_mov_b64 exec, s[66:67]
	ds_add_rtn_u32 v121, v89, v143 offset:34820
	s_mov_b64 exec, s[68:69]
	ds_add_rtn_u32 v122, v90, v143 offset:34820
	s_mov_b64 exec, s[70:71]
	ds_add_rtn_u32 v123, v91, v143 offset:34820
	s_mov_b64 exec, s[72:73]
	ds_add_rtn_u32 v124, v92, v143 offset:34820
	s_mov_b64 exec, s[74:75]
	ds_add_rtn_u32 v125, v93, v143 offset:34820
	s_mov_b64 exec, s[76:77]
	ds_add_rtn_u32 v126, v94, v143 offset:34820
	s_mov_b64 exec, s[78:79]
	ds_add_rtn_u32 v127, v95, v143 offset:34820
	s_mov_b64 exec, s[80:81]
	ds_add_rtn_u32 v128, v96, v143 offset:34820
	s_mov_b64 exec, s[82:83]
	ds_add_rtn_u32 v129, v97, v143 offset:34820
	s_mov_b64 exec, s[84:85]
	ds_add_rtn_u32 v130, v98, v143 offset:34820
	s_mov_b64 exec, s[86:87]
	ds_add_rtn_u32 v131, v99, v143 offset:34820
	s_mov_b64 exec, s[88:89]
	ds_add_rtn_u32 v132, v100, v143 offset:34820
	s_mov_b64 exec, s[90:91]
	ds_add_rtn_u32 v133, v101, v143 offset:34820
	s_mov_b64 exec, s[92:93]
	ds_add_rtn_u32 v134, v102, v143 offset:34820
	s_mov_b64 exec, s[94:95]
	ds_add_rtn_u32 v135, v103, v143 offset:34820
	s_mov_b64 exec, s[96:97]
	ds_add_rtn_u32 v136, v104, v143 offset:34820
	s_mov_b64 exec, s[98:99]
	ds_add_rtn_u32 v137, v105, v143 offset:34820
	s_mov_b64 exec, -1
	v_lshlrev_b32_e32 v145, 18, v0
	v_add_u32_e32 v146, 0x0, v145
	v_or_b32_e32 v74, v146, v74
	v_add_u32_e32 v147, 0x10000, v145
	v_or_b32_e32 v75, v147, v75
	v_add_u32_e32 v146, 0x20000, v145
	v_or_b32_e32 v76, v146, v76
	v_add_u32_e32 v147, 0x30000, v145
	v_or_b32_e32 v77, v147, v77
	v_add_u32_e32 v146, 0x4000000, v145
	v_or_b32_e32 v78, v146, v78
	v_add_u32_e32 v147, 0x4010000, v145
	v_or_b32_e32 v79, v147, v79
	v_add_u32_e32 v146, 0x4020000, v145
	v_or_b32_e32 v80, v146, v80
	v_add_u32_e32 v147, 0x4030000, v145
	v_or_b32_e32 v81, v147, v81
	v_add_u32_e32 v146, 0x8000000, v145
	v_or_b32_e32 v82, v146, v82
	v_add_u32_e32 v147, 0x8010000, v145
	v_or_b32_e32 v83, v147, v83
	v_add_u32_e32 v146, 0x8020000, v145
	v_or_b32_e32 v84, v146, v84
	v_add_u32_e32 v147, 0x8030000, v145
	v_or_b32_e32 v85, v147, v85
	v_add_u32_e32 v146, 0xc000000, v145
	v_or_b32_e32 v86, v146, v86
	v_add_u32_e32 v147, 0xc010000, v145
	v_or_b32_e32 v87, v147, v87
	v_add_u32_e32 v146, 0xc020000, v145
	v_or_b32_e32 v88, v146, v88
	v_add_u32_e32 v147, 0xc030000, v145
	v_or_b32_e32 v89, v147, v89
	v_add_u32_e32 v146, 0x10000000, v145
	v_or_b32_e32 v90, v146, v90
	v_add_u32_e32 v147, 0x10010000, v145
	v_or_b32_e32 v91, v147, v91
	v_add_u32_e32 v146, 0x10020000, v145
	v_or_b32_e32 v92, v146, v92
	v_add_u32_e32 v147, 0x10030000, v145
	v_or_b32_e32 v93, v147, v93
	v_add_u32_e32 v146, 0x14000000, v145
	v_or_b32_e32 v94, v146, v94
	v_add_u32_e32 v147, 0x14010000, v145
	v_or_b32_e32 v95, v147, v95
	v_add_u32_e32 v146, 0x14020000, v145
	v_or_b32_e32 v96, v146, v96
	v_add_u32_e32 v147, 0x14030000, v145
	v_or_b32_e32 v97, v147, v97
	v_add_u32_e32 v146, 0x18000000, v145
	v_or_b32_e32 v98, v146, v98
	v_add_u32_e32 v147, 0x18010000, v145
	v_or_b32_e32 v99, v147, v99
	v_add_u32_e32 v146, 0x18020000, v145
	v_or_b32_e32 v100, v146, v100
	v_add_u32_e32 v147, 0x18030000, v145
	v_or_b32_e32 v101, v147, v101
	v_add_u32_e32 v146, 0x1c000000, v145
	v_or_b32_e32 v102, v146, v102
	v_add_u32_e32 v147, 0x1c010000, v145
	v_or_b32_e32 v103, v147, v103
	v_add_u32_e32 v146, 0x1c020000, v145
	v_or_b32_e32 v104, v146, v104
	v_add_u32_e32 v147, 0x1c030000, v145
	v_or_b32_e32 v105, v147, v105
	s_waitcnt lgkmcnt(0)
	s_mov_b64 exec, s[36:37]
	ds_write_b32 v106, v74
	s_mov_b64 exec, s[38:39]
	ds_write_b32 v107, v75
	s_mov_b64 exec, s[40:41]
	ds_write_b32 v108, v76
	s_mov_b64 exec, s[42:43]
	ds_write_b32 v109, v77
	s_mov_b64 exec, s[44:45]
	ds_write_b32 v110, v78
	s_mov_b64 exec, s[46:47]
	ds_write_b32 v111, v79
	s_mov_b64 exec, s[48:49]
	ds_write_b32 v112, v80
	s_mov_b64 exec, s[50:51]
	ds_write_b32 v113, v81
	s_mov_b64 exec, s[52:53]
	ds_write_b32 v114, v82
	s_mov_b64 exec, s[54:55]
	ds_write_b32 v115, v83
	s_mov_b64 exec, s[56:57]
	ds_write_b32 v116, v84
	s_mov_b64 exec, s[58:59]
	ds_write_b32 v117, v85
	s_mov_b64 exec, s[60:61]
	ds_write_b32 v118, v86
	s_mov_b64 exec, s[62:63]
	ds_write_b32 v119, v87
	s_mov_b64 exec, s[64:65]
	ds_write_b32 v120, v88
	s_mov_b64 exec, s[66:67]
	ds_write_b32 v121, v89
	s_mov_b64 exec, s[68:69]
	ds_write_b32 v122, v90
	s_mov_b64 exec, s[70:71]
	ds_write_b32 v123, v91
	s_mov_b64 exec, s[72:73]
	ds_write_b32 v124, v92
	s_mov_b64 exec, s[74:75]
	ds_write_b32 v125, v93
	s_mov_b64 exec, s[76:77]
	ds_write_b32 v126, v94
	s_mov_b64 exec, s[78:79]
	ds_write_b32 v127, v95
	s_mov_b64 exec, s[80:81]
	ds_write_b32 v128, v96
	s_mov_b64 exec, s[82:83]
	ds_write_b32 v129, v97
	s_mov_b64 exec, s[84:85]
	ds_write_b32 v130, v98
	s_mov_b64 exec, s[86:87]
	ds_write_b32 v131, v99
	s_mov_b64 exec, s[88:89]
	ds_write_b32 v132, v100
	s_mov_b64 exec, s[90:91]
	ds_write_b32 v133, v101
	s_mov_b64 exec, s[92:93]
	ds_write_b32 v134, v102
	s_mov_b64 exec, s[94:95]
	ds_write_b32 v135, v103
	s_mov_b64 exec, s[96:97]
	ds_write_b32 v136, v104
	s_mov_b64 exec, s[98:99]
	ds_write_b32 v137, v105
	s_mov_b64 exec, -1
	s_waitcnt lgkmcnt(0)
	s_barrier
	s_add_i32 s53, s8, 7
	s_lshr_b32 s53, s53, 3
	v_lshlrev_b32_e32 v218, 4, v1
	v_lshlrev_b32_e32 v219, 3, v1
	v_mov_b32_e32 v223, 0x11540
	v_bfrev_b32_e32 v140, 1
	v_and_b32_e32 v221, 15, v1
	v_mov_b32_e32 v200, 0
	v_mov_b32_e32 v201, 0
	v_mov_b32_e32 v202, 0
	v_mov_b32_e32 v203, 0
	v_mov_b32_e32 v204, 0
	v_mov_b32_e32 v205, 0
	v_mov_b32_e32 v206, 0
	v_mov_b32_e32 v207, 0
	s_mov_b32 s50, -1
	s_mov_b32 s54, s17
	s_add_i32 s55, s17, 4
	s_cmp_ge_u32 s54, s53
	s_cbranch_scc1 .Lg_nochunk
	s_lshl_b32 s46, s54, 3
	v_add_u32_e32 v220, s46, v221
	v_cmp_gt_u32_e32 vcc, s8, v220
	v_lshlrev_b32_e32 v220, 2, v220
	ds_read_b32 v216, v220
	s_waitcnt lgkmcnt(0)
	v_cndmask_b32_e32 v216, v140, v216, vcc
	s_nop 1
	v_readlane_b32 s50, v216, 0
	s_and_b32 s50, s50, 0xffff
	v_readlane_b32 s40, v216, 0
	s_and_b32 s60, s40, 0xffff
	s_bitcmp1_b32 s40, 31
	s_cselect_b32 s60, 0xffff, s60
	s_bfe_u32 s40, s40, 0xd0010
	s_lshl_b32 s40, s40, 10
	s_add_u32 s42, s32, s40
	s_addc_u32 s43, s33, 0
	global_load_dwordx4 v[66:69], v218, s[42:43] nt
	v_readlane_b32 s40, v216, 1
	s_and_b32 s61, s40, 0xffff
	s_bitcmp1_b32 s40, 31
	s_cselect_b32 s61, 0xffff, s61
	s_bfe_u32 s40, s40, 0xd0010
	s_lshl_b32 s40, s40, 10
	s_add_u32 s42, s32, s40
	s_addc_u32 s43, s33, 0
	global_load_dwordx4 v[70:73], v218, s[42:43] nt
	v_readlane_b32 s40, v216, 2
	s_and_b32 s62, s40, 0xffff
	s_bitcmp1_b32 s40, 31
	s_cselect_b32 s62, 0xffff, s62
	s_bfe_u32 s40, s40, 0xd0010
	s_lshl_b32 s40, s40, 10
	s_add_u32 s42, s32, s40
	s_addc_u32 s43, s33, 0
	global_load_dwordx4 v[74:77], v218, s[42:43] nt
	v_readlane_b32 s40, v216, 3
	s_and_b32 s63, s40, 0xffff
	s_bitcmp1_b32 s40, 31
	s_cselect_b32 s63, 0xffff, s63
	s_bfe_u32 s40, s40, 0xd0010
	s_lshl_b32 s40, s40, 10
	s_add_u32 s42, s32, s40
	s_addc_u32 s43, s33, 0
	global_load_dwordx4 v[78:81], v218, s[42:43] nt
	v_readlane_b32 s40, v216, 4
	s_and_b32 s64, s40, 0xffff
	s_bitcmp1_b32 s40, 31
	s_cselect_b32 s64, 0xffff, s64
	s_bfe_u32 s40, s40, 0xd0010
	s_lshl_b32 s40, s40, 10
	s_add_u32 s42, s32, s40
	s_addc_u32 s43, s33, 0
	global_load_dwordx4 v[82:85], v218, s[42:43] nt
	v_readlane_b32 s40, v216, 5
	s_and_b32 s65, s40, 0xffff
	s_bitcmp1_b32 s40, 31
	s_cselect_b32 s65, 0xffff, s65
	s_bfe_u32 s40, s40, 0xd0010
	s_lshl_b32 s40, s40, 10
	s_add_u32 s42, s32, s40
	s_addc_u32 s43, s33, 0
	global_load_dwordx4 v[86:89], v218, s[42:43] nt
	v_readlane_b32 s40, v216, 6
	s_and_b32 s66, s40, 0xffff
	s_bitcmp1_b32 s40, 31
	s_cselect_b32 s66, 0xffff, s66
	s_bfe_u32 s40, s40, 0xd0010
	s_lshl_b32 s40, s40, 10
	s_add_u32 s42, s32, s40
	s_addc_u32 s43, s33, 0
	global_load_dwordx4 v[90:93], v218, s[42:43] nt
	v_readlane_b32 s40, v216, 7
	s_and_b32 s67, s40, 0xffff
	s_bitcmp1_b32 s40, 31
	s_cselect_b32 s67, 0xffff, s67
	s_bfe_u32 s40, s40, 0xd0010
	s_lshl_b32 s40, s40, 10
	s_add_u32 s42, s32, s40
	s_addc_u32 s43, s33, 0
	global_load_dwordx4 v[94:97], v218, s[42:43] nt
	s_cmp_ge_u32 s55, s53
	s_cbranch_scc1 .Lg_noB
	s_lshl_b32 s46, s55, 3
	v_add_u32_e32 v220, s46, v221
	v_cmp_gt_u32_e32 vcc, s8, v220
	v_lshlrev_b32_e32 v220, 2, v220
	ds_read_b32 v217, v220
	s_waitcnt lgkmcnt(0)
	v_cndmask_b32_e32 v217, v140, v217, vcc
	s_nop 1
	v_readlane_b32 s40, v217, 0
	s_and_b32 s68, s40, 0xffff
	s_bitcmp1_b32 s40, 31
	s_cselect_b32 s68, 0xffff, s68
	s_bfe_u32 s40, s40, 0xd0010
	s_lshl_b32 s40, s40, 10
	s_add_u32 s42, s32, s40
	s_addc_u32 s43, s33, 0
	global_load_dwordx4 v[98:101], v218, s[42:43] nt
	v_readlane_b32 s40, v217, 1
	s_and_b32 s69, s40, 0xffff
	s_bitcmp1_b32 s40, 31
	s_cselect_b32 s69, 0xffff, s69
	s_bfe_u32 s40, s40, 0xd0010
	s_lshl_b32 s40, s40, 10
	s_add_u32 s42, s32, s40
	s_addc_u32 s43, s33, 0
	global_load_dwordx4 v[102:105], v218, s[42:43] nt
	v_readlane_b32 s40, v217, 2
	s_and_b32 s70, s40, 0xffff
	s_bitcmp1_b32 s40, 31
	s_cselect_b32 s70, 0xffff, s70
	s_bfe_u32 s40, s40, 0xd0010
	s_lshl_b32 s40, s40, 10
	s_add_u32 s42, s32, s40
	s_addc_u32 s43, s33, 0
	global_load_dwordx4 v[106:109], v218, s[42:43] nt
	v_readlane_b32 s40, v217, 3
	s_and_b32 s71, s40, 0xffff
	s_bitcmp1_b32 s40, 31
	s_cselect_b32 s71, 0xffff, s71
	s_bfe_u32 s40, s40, 0xd0010
	s_lshl_b32 s40, s40, 10
	s_add_u32 s42, s32, s40
	s_addc_u32 s43, s33, 0
	global_load_dwordx4 v[110:113], v218, s[42:43] nt
	v_readlane_b32 s40, v217, 4
	s_and_b32 s72, s40, 0xffff
	s_bitcmp1_b32 s40, 31
	s_cselect_b32 s72, 0xffff, s72
	s_bfe_u32 s40, s40, 0xd0010
	s_lshl_b32 s40, s40, 10
	s_add_u32 s42, s32, s40
	s_addc_u32 s43, s33, 0
	global_load_dwordx4 v[114:117], v218, s[42:43] nt
	v_readlane_b32 s40, v217, 5
	s_and_b32 s73, s40, 0xffff
	s_bitcmp1_b32 s40, 31
	s_cselect_b32 s73, 0xffff, s73
	s_bfe_u32 s40, s40, 0xd0010
	s_lshl_b32 s40, s40, 10
	s_add_u32 s42, s32, s40
	s_addc_u32 s43, s33, 0
	global_load_dwordx4 v[118:121], v218, s[42:43] nt
	v_readlane_b32 s40, v217, 6
	s_and_b32 s74, s40, 0xffff
	s_bitcmp1_b32 s40, 31
	s_cselect_b32 s74, 0xffff, s74
	s_bfe_u32 s40, s40, 0xd0010
	s_lshl_b32 s40, s40, 10
	s_add_u32 s42, s32, s40
	s_addc_u32 s43, s33, 0
	global_load_dwordx4 v[122:125], v218, s[42:43] nt
	v_readlane_b32 s40, v217, 7
	s_and_b32 s75, s40, 0xffff
	s_bitcmp1_b32 s40, 31
	s_cselect_b32 s75, 0xffff, s75
	s_bfe_u32 s40, s40, 0xd0010
	s_lshl_b32 s40, s40, 10
	s_add_u32 s42, s32, s40
	s_addc_u32 s43, s33, 0
	global_load_dwordx4 v[126:129], v218, s[42:43] nt
.Lg_loop:
	s_mov_b64 exec, 1
	ds_add_rtn_u32 v222, v223, v142
	s_mov_b64 exec, -1
	s_waitcnt vmcnt(15)
	s_cmp_eq_u32 s60, 0xffff
	s_cbranch_scc1 .Lc_A8_skip0
	s_cmp_lg_u32 s60, s50
	s_cbranch_scc1 .Lc_A8_flush0

.Lc_A8_skip0:
	s_waitcnt vmcnt(14)
	s_cmp_eq_u32 s61, 0xffff
	s_cbranch_scc1 .Lc_A8_skip1
	s_cmp_lg_u32 s61, s50
	s_cbranch_scc1 .Lc_A8_flush1

.Lc_A8_skip1:
	s_waitcnt vmcnt(13)
	s_cmp_eq_u32 s62, 0xffff
	s_cbranch_scc1 .Lc_A8_skip2
	s_cmp_lg_u32 s62, s50
	s_cbranch_scc1 .Lc_A8_flush2

.Lc_A8_skip2:
	s_waitcnt vmcnt(12)
	s_cmp_eq_u32 s63, 0xffff
	s_cbranch_scc1 .Lc_A8_skip3
	s_cmp_lg_u32 s63, s50
	s_cbranch_scc1 .Lc_A8_flush3

.Lc_A8_skip3:
	s_waitcnt vmcnt(11)
	s_cmp_eq_u32 s64, 0xffff
	s_cbranch_scc1 .Lc_A8_skip4
	s_cmp_lg_u32 s64, s50
	s_cbranch_scc1 .Lc_A8_flush4

.Lc_A8_skip4:
	s_waitcnt vmcnt(10)
	s_cmp_eq_u32 s65, 0xffff
	s_cbranch_scc1 .Lc_A8_skip5
	s_cmp_lg_u32 s65, s50
	s_cbranch_scc1 .Lc_A8_flush5

.Lc_A8_skip5:
	s_waitcnt vmcnt(9)
	s_cmp_eq_u32 s66, 0xffff
	s_cbranch_scc1 .Lc_A8_skip6
	s_cmp_lg_u32 s66, s50
	s_cbranch_scc1 .Lc_A8_flush6

.Lc_A8_skip6:
	s_waitcnt vmcnt(8)
	s_cmp_eq_u32 s67, 0xffff
	s_cbranch_scc1 .Lc_A8_skip7
	s_cmp_lg_u32 s67, s50
	s_cbranch_scc1 .Lc_A8_flush7

.Lc_A8_skip7:
	s_waitcnt lgkmcnt(0)
	v_readfirstlane_b32 s54, v222
	s_cmp_ge_u32 s54, s53
	s_cbranch_scc1 .Lg_drainB
	s_lshl_b32 s46, s54, 3
	v_add_u32_e32 v220, s46, v221
	v_cmp_gt_u32_e32 vcc, s8, v220
	v_lshlrev_b32_e32 v220, 2, v220
	ds_read_b32 v216, v220
	s_waitcnt lgkmcnt(0)
	v_cndmask_b32_e32 v216, v140, v216, vcc
	s_nop 1
	v_readlane_b32 s40, v216, 0
	s_and_b32 s60, s40, 0xffff
	s_bitcmp1_b32 s40, 31
	s_cselect_b32 s60, 0xffff, s60
	s_bfe_u32 s40, s40, 0xd0010
	s_lshl_b32 s40, s40, 10
	s_add_u32 s42, s32, s40
	s_addc_u32 s43, s33, 0
	global_load_dwordx4 v[66:69], v218, s[42:43] nt
	v_readlane_b32 s40, v216, 1
	s_and_b32 s61, s40, 0xffff
	s_bitcmp1_b32 s40, 31
	s_cselect_b32 s61, 0xffff, s61
	s_bfe_u32 s40, s40, 0xd0010
	s_lshl_b32 s40, s40, 10
	s_add_u32 s42, s32, s40
	s_addc_u32 s43, s33, 0
	global_load_dwordx4 v[70:73], v218, s[42:43] nt
	v_readlane_b32 s40, v216, 2
	s_and_b32 s62, s40, 0xffff
	s_bitcmp1_b32 s40, 31
	s_cselect_b32 s62, 0xffff, s62
	s_bfe_u32 s40, s40, 0xd0010
	s_lshl_b32 s40, s40, 10
	s_add_u32 s42, s32, s40
	s_addc_u32 s43, s33, 0
	global_load_dwordx4 v[74:77], v218, s[42:43] nt
	v_readlane_b32 s40, v216, 3
	s_and_b32 s63, s40, 0xffff
	s_bitcmp1_b32 s40, 31
	s_cselect_b32 s63, 0xffff, s63
	s_bfe_u32 s40, s40, 0xd0010
	s_lshl_b32 s40, s40, 10
	s_add_u32 s42, s32, s40
	s_addc_u32 s43, s33, 0
	global_load_dwordx4 v[78:81], v218, s[42:43] nt
	v_readlane_b32 s40, v216, 4
	s_and_b32 s64, s40, 0xffff
	s_bitcmp1_b32 s40, 31
	s_cselect_b32 s64, 0xffff, s64
	s_bfe_u32 s40, s40, 0xd0010
	s_lshl_b32 s40, s40, 10
	s_add_u32 s42, s32, s40
	s_addc_u32 s43, s33, 0
	global_load_dwordx4 v[82:85], v218, s[42:43] nt
	v_readlane_b32 s40, v216, 5
	s_and_b32 s65, s40, 0xffff
	s_bitcmp1_b32 s40, 31
	s_cselect_b32 s65, 0xffff, s65
	s_bfe_u32 s40, s40, 0xd0010
	s_lshl_b32 s40, s40, 10
	s_add_u32 s42, s32, s40
	s_addc_u32 s43, s33, 0
	global_load_dwordx4 v[86:89], v218, s[42:43] nt
	v_readlane_b32 s40, v216, 6
	s_and_b32 s66, s40, 0xffff
	s_bitcmp1_b32 s40, 31
	s_cselect_b32 s66, 0xffff, s66
	s_bfe_u32 s40, s40, 0xd0010
	s_lshl_b32 s40, s40, 10
	s_add_u32 s42, s32, s40
	s_addc_u32 s43, s33, 0
	global_load_dwordx4 v[90:93], v218, s[42:43] nt
	v_readlane_b32 s40, v216, 7
	s_and_b32 s67, s40, 0xffff
	s_bitcmp1_b32 s40, 31
	s_cselect_b32 s67, 0xffff, s67
	s_bfe_u32 s40, s40, 0xd0010
	s_lshl_b32 s40, s40, 10
	s_add_u32 s42, s32, s40
	s_addc_u32 s43, s33, 0
	global_load_dwordx4 v[94:97], v218, s[42:43] nt
	s_mov_b64 exec, 1
	ds_add_rtn_u32 v222, v223, v142
	s_mov_b64 exec, -1
	s_waitcnt vmcnt(15)
	s_cmp_eq_u32 s68, 0xffff
	s_cbranch_scc1 .Lc_B8_skip8
	s_cmp_lg_u32 s68, s50
	s_cbranch_scc1 .Lc_B8_flush8

.Lc_B8_skip8:
	s_waitcnt vmcnt(14)
	s_cmp_eq_u32 s69, 0xffff
	s_cbranch_scc1 .Lc_B8_skip9
	s_cmp_lg_u32 s69, s50
	s_cbranch_scc1 .Lc_B8_flush9

.Lc_B8_skip9:
	s_waitcnt vmcnt(13)
	s_cmp_eq_u32 s70, 0xffff
	s_cbranch_scc1 .Lc_B8_skip10
	s_cmp_lg_u32 s70, s50
	s_cbranch_scc1 .Lc_B8_flush10

.Lc_B8_skip10:
	s_waitcnt vmcnt(12)
	s_cmp_eq_u32 s71, 0xffff
	s_cbranch_scc1 .Lc_B8_skip11
	s_cmp_lg_u32 s71, s50
	s_cbranch_scc1 .Lc_B8_flush11

.Lc_B8_skip11:
	s_waitcnt vmcnt(11)
	s_cmp_eq_u32 s72, 0xffff
	s_cbranch_scc1 .Lc_B8_skip12
	s_cmp_lg_u32 s72, s50
	s_cbranch_scc1 .Lc_B8_flush12

.Lc_B8_skip12:
	s_waitcnt vmcnt(10)
	s_cmp_eq_u32 s73, 0xffff
	s_cbranch_scc1 .Lc_B8_skip13
	s_cmp_lg_u32 s73, s50
	s_cbranch_scc1 .Lc_B8_flush13

.Lc_B8_skip13:
	s_waitcnt vmcnt(9)
	s_cmp_eq_u32 s74, 0xffff
	s_cbranch_scc1 .Lc_B8_skip14
	s_cmp_lg_u32 s74, s50
	s_cbranch_scc1 .Lc_B8_flush14

.Lc_B8_skip14:
	s_waitcnt vmcnt(8)
	s_cmp_eq_u32 s75, 0xffff
	s_cbranch_scc1 .Lc_B8_skip15
	s_cmp_lg_u32 s75, s50
	s_cbranch_scc1 .Lc_B8_flush15

.Lc_B8_skip15:
	s_waitcnt lgkmcnt(0)
	v_readfirstlane_b32 s55, v222
	s_cmp_ge_u32 s55, s53
	s_cbranch_scc1 .Lg_drainA
	s_lshl_b32 s46, s55, 3
	v_add_u32_e32 v220, s46, v221
	v_cmp_gt_u32_e32 vcc, s8, v220
	v_lshlrev_b32_e32 v220, 2, v220
	ds_read_b32 v217, v220
	s_waitcnt lgkmcnt(0)
	v_cndmask_b32_e32 v217, v140, v217, vcc
	s_nop 1
	v_readlane_b32 s40, v217, 0
	s_and_b32 s68, s40, 0xffff
	s_bitcmp1_b32 s40, 31
	s_cselect_b32 s68, 0xffff, s68
	s_bfe_u32 s40, s40, 0xd0010
	s_lshl_b32 s40, s40, 10
	s_add_u32 s42, s32, s40
	s_addc_u32 s43, s33, 0
	global_load_dwordx4 v[98:101], v218, s[42:43] nt
	v_readlane_b32 s40, v217, 1
	s_and_b32 s69, s40, 0xffff
	s_bitcmp1_b32 s40, 31
	s_cselect_b32 s69, 0xffff, s69
	s_bfe_u32 s40, s40, 0xd0010
	s_lshl_b32 s40, s40, 10
	s_add_u32 s42, s32, s40
	s_addc_u32 s43, s33, 0
	global_load_dwordx4 v[102:105], v218, s[42:43] nt
	v_readlane_b32 s40, v217, 2
	s_and_b32 s70, s40, 0xffff
	s_bitcmp1_b32 s40, 31
	s_cselect_b32 s70, 0xffff, s70
	s_bfe_u32 s40, s40, 0xd0010
	s_lshl_b32 s40, s40, 10
	s_add_u32 s42, s32, s40
	s_addc_u32 s43, s33, 0
	global_load_dwordx4 v[106:109], v218, s[42:43] nt
	v_readlane_b32 s40, v217, 3
	s_and_b32 s71, s40, 0xffff
	s_bitcmp1_b32 s40, 31
	s_cselect_b32 s71, 0xffff, s71
	s_bfe_u32 s40, s40, 0xd0010
	s_lshl_b32 s40, s40, 10
	s_add_u32 s42, s32, s40
	s_addc_u32 s43, s33, 0
	global_load_dwordx4 v[110:113], v218, s[42:43] nt
	v_readlane_b32 s40, v217, 4
	s_and_b32 s72, s40, 0xffff
	s_bitcmp1_b32 s40, 31
	s_cselect_b32 s72, 0xffff, s72
	s_bfe_u32 s40, s40, 0xd0010
	s_lshl_b32 s40, s40, 10
	s_add_u32 s42, s32, s40
	s_addc_u32 s43, s33, 0
	global_load_dwordx4 v[114:117], v218, s[42:43] nt
	v_readlane_b32 s40, v217, 5
	s_and_b32 s73, s40, 0xffff
	s_bitcmp1_b32 s40, 31
	s_cselect_b32 s73, 0xffff, s73
	s_bfe_u32 s40, s40, 0xd0010
	s_lshl_b32 s40, s40, 10
	s_add_u32 s42, s32, s40
	s_addc_u32 s43, s33, 0
	global_load_dwordx4 v[118:121], v218, s[42:43] nt
	v_readlane_b32 s40, v217, 6
	s_and_b32 s74, s40, 0xffff
	s_bitcmp1_b32 s40, 31
	s_cselect_b32 s74, 0xffff, s74
	s_bfe_u32 s40, s40, 0xd0010
	s_lshl_b32 s40, s40, 10
	s_add_u32 s42, s32, s40
	s_addc_u32 s43, s33, 0
	global_load_dwordx4 v[122:125], v218, s[42:43] nt
	v_readlane_b32 s40, v217, 7
	s_and_b32 s75, s40, 0xffff
	s_bitcmp1_b32 s40, 31
	s_cselect_b32 s75, 0xffff, s75
	s_bfe_u32 s40, s40, 0xd0010
	s_lshl_b32 s40, s40, 10
	s_add_u32 s42, s32, s40
	s_addc_u32 s43, s33, 0
	global_load_dwordx4 v[126:129], v218, s[42:43] nt
	s_branch .Lg_loop
.Lg_noB:
.Lg_drainA:
	s_waitcnt vmcnt(7)
	s_cmp_eq_u32 s60, 0xffff
	s_cbranch_scc1 .Lc_A0_skip0
	s_cmp_lg_u32 s60, s50
	s_cbranch_scc1 .Lc_A0_flush0

.Lc_A0_skip0:
	s_waitcnt vmcnt(6)
	s_cmp_eq_u32 s61, 0xffff
	s_cbranch_scc1 .Lc_A0_skip1
	s_cmp_lg_u32 s61, s50
	s_cbranch_scc1 .Lc_A0_flush1

.Lc_A0_skip1:
	s_waitcnt vmcnt(5)
	s_cmp_eq_u32 s62, 0xffff
	s_cbranch_scc1 .Lc_A0_skip2
	s_cmp_lg_u32 s62, s50
	s_cbranch_scc1 .Lc_A0_flush2

.Lc_A0_skip2:
	s_waitcnt vmcnt(4)
	s_cmp_eq_u32 s63, 0xffff
	s_cbranch_scc1 .Lc_A0_skip3
	s_cmp_lg_u32 s63, s50
	s_cbranch_scc1 .Lc_A0_flush3

.Lc_A0_skip3:
	s_waitcnt vmcnt(3)
	s_cmp_eq_u32 s64, 0xffff
	s_cbranch_scc1 .Lc_A0_skip4
	s_cmp_lg_u32 s64, s50
	s_cbranch_scc1 .Lc_A0_flush4

.Lc_A0_skip4:
	s_waitcnt vmcnt(2)
	s_cmp_eq_u32 s65, 0xffff
	s_cbranch_scc1 .Lc_A0_skip5
	s_cmp_lg_u32 s65, s50
	s_cbranch_scc1 .Lc_A0_flush5

.Lc_A0_skip5:
	s_waitcnt vmcnt(1)
	s_cmp_eq_u32 s66, 0xffff
	s_cbranch_scc1 .Lc_A0_skip6
	s_cmp_lg_u32 s66, s50
	s_cbranch_scc1 .Lc_A0_flush6

.Lc_A0_skip6:
	s_waitcnt vmcnt(0)
	s_cmp_eq_u32 s67, 0xffff
	s_cbranch_scc1 .Lc_A0_skip7
	s_cmp_lg_u32 s67, s50
	s_cbranch_scc1 .Lc_A0_flush7

.Lg_drainB:
	s_waitcnt vmcnt(7)
	s_cmp_eq_u32 s68, 0xffff
	s_cbranch_scc1 .Lc_B0_skip8
	s_cmp_lg_u32 s68, s50
	s_cbranch_scc1 .Lc_B0_flush8

.Lc_B0_skip8:
	s_waitcnt vmcnt(6)
	s_cmp_eq_u32 s69, 0xffff
	s_cbranch_scc1 .Lc_B0_skip9
	s_cmp_lg_u32 s69, s50
	s_cbranch_scc1 .Lc_B0_flush9

.Lc_B0_skip9:
	s_waitcnt vmcnt(5)
	s_cmp_eq_u32 s70, 0xffff
	s_cbranch_scc1 .Lc_B0_skip10
	s_cmp_lg_u32 s70, s50
	s_cbranch_scc1 .Lc_B0_flush10

.Lc_B0_skip10:
	s_waitcnt vmcnt(4)
	s_cmp_eq_u32 s71, 0xffff
	s_cbranch_scc1 .Lc_B0_skip11
	s_cmp_lg_u32 s71, s50
	s_cbranch_scc1 .Lc_B0_flush11

.Lc_B0_skip11:
	s_waitcnt vmcnt(3)
	s_cmp_eq_u32 s72, 0xffff
	s_cbranch_scc1 .Lc_B0_skip12
	s_cmp_lg_u32 s72, s50
	s_cbranch_scc1 .Lc_B0_flush12

.Lc_B0_skip12:
	s_waitcnt vmcnt(2)
	s_cmp_eq_u32 s73, 0xffff
	s_cbranch_scc1 .Lc_B0_skip13
	s_cmp_lg_u32 s73, s50
	s_cbranch_scc1 .Lc_B0_flush13

.Lc_B0_skip13:
	s_waitcnt vmcnt(1)
	s_cmp_eq_u32 s74, 0xffff
	s_cbranch_scc1 .Lc_B0_skip14
	s_cmp_lg_u32 s74, s50
	s_cbranch_scc1 .Lc_B0_flush14

.Lc_B0_skip14:
	s_waitcnt vmcnt(0)
	s_cmp_eq_u32 s75, 0xffff
	s_cbranch_scc1 .Lc_B0_skip15
	s_cmp_lg_u32 s75, s50
	s_cbranch_scc1 .Lc_B0_flush15

.Lc_B0_skip15:
.Lg_fin:
	v_add_u32_e32 v220, s50, v219
	ds_add_f64 v220, v[200:201] offset:32768
	ds_add_f64 v220, v[202:203] offset:33280
	ds_add_f64 v220, v[204:205] offset:33792
	ds_add_f64 v220, v[206:207] offset:34304
	s_branch .Lg_alldone

.Lc_A8_flush0:
	v_add_u32_e32 v220, s50, v219
	ds_add_f64 v220, v[200:201] offset:32768
	ds_add_f64 v220, v[202:203] offset:33280
	ds_add_f64 v220, v[204:205] offset:33792
	ds_add_f64 v220, v[206:207] offset:34304
	v_mov_b32_e32 v200, 0
	v_mov_b32_e32 v201, 0
	v_mov_b32_e32 v202, 0
	v_mov_b32_e32 v203, 0
	v_mov_b32_e32 v204, 0
	v_mov_b32_e32 v205, 0
	v_mov_b32_e32 v206, 0
	v_mov_b32_e32 v207, 0
	s_mov_b32 s50, s60
	s_branch .Lc_A8_cont0
.Lc_A8_flush1:
	v_add_u32_e32 v220, s50, v219
	ds_add_f64 v220, v[200:201] offset:32768
	ds_add_f64 v220, v[202:203] offset:33280
	ds_add_f64 v220, v[204:205] offset:33792
	ds_add_f64 v220, v[206:207] offset:34304
	v_mov_b32_e32 v200, 0
	v_mov_b32_e32 v201, 0
	v_mov_b32_e32 v202, 0
	v_mov_b32_e32 v203, 0
	v_mov_b32_e32 v204, 0
	v_mov_b32_e32 v205, 0
	v_mov_b32_e32 v206, 0
	v_mov_b32_e32 v207, 0
	s_mov_b32 s50, s61
	s_branch .Lc_A8_cont1
.Lc_A8_flush2:
	v_add_u32_e32 v220, s50, v219
	ds_add_f64 v220, v[200:201] offset:32768
	ds_add_f64 v220, v[202:203] offset:33280
	ds_add_f64 v220, v[204:205] offset:33792
	ds_add_f64 v220, v[206:207] offset:34304
	v_mov_b32_e32 v200, 0
	v_mov_b32_e32 v201, 0
	v_mov_b32_e32 v202, 0
	v_mov_b32_e32 v203, 0
	v_mov_b32_e32 v204, 0
	v_mov_b32_e32 v205, 0
	v_mov_b32_e32 v206, 0
	v_mov_b32_e32 v207, 0
	s_mov_b32 s50, s62
	s_branch .Lc_A8_cont2
.Lc_A8_flush3:
	v_add_u32_e32 v220, s50, v219
	ds_add_f64 v220, v[200:201] offset:32768
	ds_add_f64 v220, v[202:203] offset:33280
	ds_add_f64 v220, v[204:205] offset:33792
	ds_add_f64 v220, v[206:207] offset:34304
	v_mov_b32_e32 v200, 0
	v_mov_b32_e32 v201, 0
	v_mov_b32_e32 v202, 0
	v_mov_b32_e32 v203, 0
	v_mov_b32_e32 v204, 0
	v_mov_b32_e32 v205, 0
	v_mov_b32_e32 v206, 0
	v_mov_b32_e32 v207, 0
	s_mov_b32 s50, s63
	s_branch .Lc_A8_cont3
.Lc_A8_flush4:
	v_add_u32_e32 v220, s50, v219
	ds_add_f64 v220, v[200:201] offset:32768
	ds_add_f64 v220, v[202:203] offset:33280
	ds_add_f64 v220, v[204:205] offset:33792
	ds_add_f64 v220, v[206:207] offset:34304
	v_mov_b32_e32 v200, 0
	v_mov_b32_e32 v201, 0
	v_mov_b32_e32 v202, 0
	v_mov_b32_e32 v203, 0
	v_mov_b32_e32 v204, 0
	v_mov_b32_e32 v205, 0
	v_mov_b32_e32 v206, 0
	v_mov_b32_e32 v207, 0
	s_mov_b32 s50, s64
	s_branch .Lc_A8_cont4
.Lc_A8_flush5:
	v_add_u32_e32 v220, s50, v219
	ds_add_f64 v220, v[200:201] offset:32768
	ds_add_f64 v220, v[202:203] offset:33280
	ds_add_f64 v220, v[204:205] offset:33792
	ds_add_f64 v220, v[206:207] offset:34304
	v_mov_b32_e32 v200, 0
	v_mov_b32_e32 v201, 0
	v_mov_b32_e32 v202, 0
	v_mov_b32_e32 v203, 0
	v_mov_b32_e32 v204, 0
	v_mov_b32_e32 v205, 0
	v_mov_b32_e32 v206, 0
	v_mov_b32_e32 v207, 0
	s_mov_b32 s50, s65
	s_branch .Lc_A8_cont5
.Lc_A8_flush6:
	v_add_u32_e32 v220, s50, v219
	ds_add_f64 v220, v[200:201] offset:32768
	ds_add_f64 v220, v[202:203] offset:33280
	ds_add_f64 v220, v[204:205] offset:33792
	ds_add_f64 v220, v[206:207] offset:34304
	v_mov_b32_e32 v200, 0
	v_mov_b32_e32 v201, 0
	v_mov_b32_e32 v202, 0
	v_mov_b32_e32 v203, 0
	v_mov_b32_e32 v204, 0
	v_mov_b32_e32 v205, 0
	v_mov_b32_e32 v206, 0
	v_mov_b32_e32 v207, 0
	s_mov_b32 s50, s66
	s_branch .Lc_A8_cont6
.Lc_A8_flush7:
	v_add_u32_e32 v220, s50, v219
	ds_add_f64 v220, v[200:201] offset:32768
	ds_add_f64 v220, v[202:203] offset:33280
	ds_add_f64 v220, v[204:205] offset:33792
	ds_add_f64 v220, v[206:207] offset:34304
	v_mov_b32_e32 v200, 0
	v_mov_b32_e32 v201, 0
	v_mov_b32_e32 v202, 0
	v_mov_b32_e32 v203, 0
	v_mov_b32_e32 v204, 0
	v_mov_b32_e32 v205, 0
	v_mov_b32_e32 v206, 0
	v_mov_b32_e32 v207, 0
	s_mov_b32 s50, s67
	s_branch .Lc_A8_cont7
.Lc_B8_flush8:
	v_add_u32_e32 v220, s50, v219
	ds_add_f64 v220, v[200:201] offset:32768
	ds_add_f64 v220, v[202:203] offset:33280
	ds_add_f64 v220, v[204:205] offset:33792
	ds_add_f64 v220, v[206:207] offset:34304
	v_mov_b32_e32 v200, 0
	v_mov_b32_e32 v201, 0
	v_mov_b32_e32 v202, 0
	v_mov_b32_e32 v203, 0
	v_mov_b32_e32 v204, 0
	v_mov_b32_e32 v205, 0
	v_mov_b32_e32 v206, 0
	v_mov_b32_e32 v207, 0
	s_mov_b32 s50, s68
	s_branch .Lc_B8_cont8
.Lc_B8_flush9:
	v_add_u32_e32 v220, s50, v219
	ds_add_f64 v220, v[200:201] offset:32768
	ds_add_f64 v220, v[202:203] offset:33280
	ds_add_f64 v220, v[204:205] offset:33792
	ds_add_f64 v220, v[206:207] offset:34304
	v_mov_b32_e32 v200, 0
	v_mov_b32_e32 v201, 0
	v_mov_b32_e32 v202, 0
	v_mov_b32_e32 v203, 0
	v_mov_b32_e32 v204, 0
	v_mov_b32_e32 v205, 0
	v_mov_b32_e32 v206, 0
	v_mov_b32_e32 v207, 0
	s_mov_b32 s50, s69
	s_branch .Lc_B8_cont9
.Lc_B8_flush10:
	v_add_u32_e32 v220, s50, v219
	ds_add_f64 v220, v[200:201] offset:32768
	ds_add_f64 v220, v[202:203] offset:33280
	ds_add_f64 v220, v[204:205] offset:33792
	ds_add_f64 v220, v[206:207] offset:34304
	v_mov_b32_e32 v200, 0
	v_mov_b32_e32 v201, 0
	v_mov_b32_e32 v202, 0
	v_mov_b32_e32 v203, 0
	v_mov_b32_e32 v204, 0
	v_mov_b32_e32 v205, 0
	v_mov_b32_e32 v206, 0
	v_mov_b32_e32 v207, 0
	s_mov_b32 s50, s70
	s_branch .Lc_B8_cont10
.Lc_B8_flush11:
	v_add_u32_e32 v220, s50, v219
	ds_add_f64 v220, v[200:201] offset:32768
	ds_add_f64 v220, v[202:203] offset:33280
	ds_add_f64 v220, v[204:205] offset:33792
	ds_add_f64 v220, v[206:207] offset:34304
	v_mov_b32_e32 v200, 0
	v_mov_b32_e32 v201, 0
	v_mov_b32_e32 v202, 0
	v_mov_b32_e32 v203, 0
	v_mov_b32_e32 v204, 0
	v_mov_b32_e32 v205, 0
	v_mov_b32_e32 v206, 0
	v_mov_b32_e32 v207, 0
	s_mov_b32 s50, s71
	s_branch .Lc_B8_cont11
.Lc_B8_flush12:
	v_add_u32_e32 v220, s50, v219
	ds_add_f64 v220, v[200:201] offset:32768
	ds_add_f64 v220, v[202:203] offset:33280
	ds_add_f64 v220, v[204:205] offset:33792
	ds_add_f64 v220, v[206:207] offset:34304
	v_mov_b32_e32 v200, 0
	v_mov_b32_e32 v201, 0
	v_mov_b32_e32 v202, 0
	v_mov_b32_e32 v203, 0
	v_mov_b32_e32 v204, 0
	v_mov_b32_e32 v205, 0
	v_mov_b32_e32 v206, 0
	v_mov_b32_e32 v207, 0
	s_mov_b32 s50, s72
	s_branch .Lc_B8_cont12
.Lc_B8_flush13:
	v_add_u32_e32 v220, s50, v219
	ds_add_f64 v220, v[200:201] offset:32768
	ds_add_f64 v220, v[202:203] offset:33280
	ds_add_f64 v220, v[204:205] offset:33792
	ds_add_f64 v220, v[206:207] offset:34304
	v_mov_b32_e32 v200, 0
	v_mov_b32_e32 v201, 0
	v_mov_b32_e32 v202, 0
	v_mov_b32_e32 v203, 0
	v_mov_b32_e32 v204, 0
	v_mov_b32_e32 v205, 0
	v_mov_b32_e32 v206, 0
	v_mov_b32_e32 v207, 0
	s_mov_b32 s50, s73
	s_branch .Lc_B8_cont13
.Lc_B8_flush14:
	v_add_u32_e32 v220, s50, v219
	ds_add_f64 v220, v[200:201] offset:32768
	ds_add_f64 v220, v[202:203] offset:33280
	ds_add_f64 v220, v[204:205] offset:33792
	ds_add_f64 v220, v[206:207] offset:34304
	v_mov_b32_e32 v200, 0
	v_mov_b32_e32 v201, 0
	v_mov_b32_e32 v202, 0
	v_mov_b32_e32 v203, 0
	v_mov_b32_e32 v204, 0
	v_mov_b32_e32 v205, 0
	v_mov_b32_e32 v206, 0
	v_mov_b32_e32 v207, 0
	s_mov_b32 s50, s74
	s_branch .Lc_B8_cont14
.Lc_B8_flush15:
	v_add_u32_e32 v220, s50, v219
	ds_add_f64 v220, v[200:201] offset:32768
	ds_add_f64 v220, v[202:203] offset:33280
	ds_add_f64 v220, v[204:205] offset:33792
	ds_add_f64 v220, v[206:207] offset:34304
	v_mov_b32_e32 v200, 0
	v_mov_b32_e32 v201, 0
	v_mov_b32_e32 v202, 0
	v_mov_b32_e32 v203, 0
	v_mov_b32_e32 v204, 0
	v_mov_b32_e32 v205, 0
	v_mov_b32_e32 v206, 0
	v_mov_b32_e32 v207, 0
	s_mov_b32 s50, s75
	s_branch .Lc_B8_cont15

.Lg_alldone:
	s_cmp_lg_u32 s17, 0
	s_cbranch_scc1 .Lg_nocopy
	v_cmp_gt_u32_e32 vcc, 16, v1
	s_and_saveexec_b64 s[30:31], vcc
	v_mul_u32_u24_e32 v220, 0x810, v1
	ds_read_b32 v221, v220 offset:34816
	v_lshl_add_u32 v220, v1, 2, v144
	s_waitcnt lgkmcnt(0)
	ds_write_b32 v220, v221
	s_mov_b64 exec, s[30:31]
